# grid barrier: non-leader workgroups poll the cross-XCD release generation directly (one polling hop less per seam), own agent-scope acquire unchanged
# speedup vs baseline: 1.0075x; 1.0075x over previous
.LBB0_285:
	v_readlane_b32 s4, v253, 55
	v_readlane_b32 s5, v253, 56
	v_cvt_f32_u32_e32 v3, v5
	v_sub_u32_e32 v7, 0, v5
	v_rcp_iflag_f32_e32 v3, v3
	s_nop 1
	global_atomic_add v6, v4, v201, s[4:5] sc0
	v_mul_f32_e32 v3, 0x4f7ffffe, v3
	v_cvt_u32_f32_e32 v3, v3
	v_mul_lo_u32 v7, v7, v3
	v_mul_hi_u32 v7, v3, v7
	v_add_u32_e32 v3, v3, v7
	s_waitcnt vmcnt(0)
	v_mul_hi_u32 v3, v6, v3
	v_mul_lo_u32 v7, v3, v5
	v_sub_u32_e32 v7, v6, v7
	v_add_u32_e32 v8, 1, v3
	v_cmp_ge_u32_e32 vcc, v7, v5
	v_add_u32_e32 v6, 1, v6
	s_nop 0
	v_cndmask_b32_e32 v3, v3, v8, vcc
	v_sub_u32_e32 v8, v7, v5
	v_cndmask_b32_e32 v7, v7, v8, vcc
	v_add_u32_e32 v8, 1, v3
	v_cmp_ge_u32_e32 vcc, v7, v5
	s_nop 1
	v_cndmask_b32_e32 v3, v3, v8, vcc
	v_mul_lo_u32 v7, v5, v3
	v_add_u32_e32 v5, v7, v5
	v_cmp_ne_u32_e32 vcc, v6, v5
	s_and_saveexec_b64 s[8:9], vcc
	s_xor_b64 s[8:9], exec, s[8:9]
	s_cbranch_execz .LBB0_299
	v_readlane_b32 s4, v253, 61
	v_readlane_b32 s5, v253, 62
	s_waitcnt lgkmcnt(0)
	s_nop 3
	global_load_dword v2, v4, s[4:5] sc1
	s_waitcnt vmcnt(0)
	v_cmp_eq_u32_e32 vcc, v2, v3
	s_and_saveexec_b64 s[10:11], vcc
	s_cbranch_execz .LBB0_298
	s_mov_b32 s5, 1
	s_mov_b64 s[12:13], 0
	s_branch .LBB0_289

.LBB0_291:
	v_readlane_b32 s16, v253, 61
	v_readlane_b32 s17, v253, 62
	s_add_i32 s5, s5, 1
	s_mov_b64 s[18:19], -1
	s_nop 2
	global_load_dword v2, v4, s[16:17] sc1
	s_waitcnt vmcnt(0)
	v_cmp_ne_u32_e32 vcc, v2, v3
	s_orn2_b64 s[16:17], vcc, exec
	s_branch .LBB0_288

.LBB0_468:
	v_readlane_b32 s8, v253, 55
	v_readlane_b32 s9, v253, 56
	v_cvt_f32_u32_e32 v3, v5
	v_sub_u32_e32 v7, 0, v5
	v_rcp_iflag_f32_e32 v3, v3
	s_nop 1
	global_atomic_add v6, v4, v201, s[8:9] sc0
	v_mul_f32_e32 v3, 0x4f7ffffe, v3
	v_cvt_u32_f32_e32 v3, v3
	v_mul_lo_u32 v7, v7, v3
	v_mul_hi_u32 v7, v3, v7
	v_add_u32_e32 v3, v3, v7
	s_waitcnt vmcnt(0)
	v_mul_hi_u32 v3, v6, v3
	v_mul_lo_u32 v7, v3, v5
	v_sub_u32_e32 v7, v6, v7
	v_add_u32_e32 v8, 1, v3
	v_cmp_ge_u32_e32 vcc, v7, v5
	v_add_u32_e32 v6, 1, v6
	s_nop 0
	v_cndmask_b32_e32 v3, v3, v8, vcc
	v_sub_u32_e32 v8, v7, v5
	v_cndmask_b32_e32 v7, v7, v8, vcc
	v_add_u32_e32 v8, 1, v3
	v_cmp_ge_u32_e32 vcc, v7, v5
	s_nop 1
	v_cndmask_b32_e32 v3, v3, v8, vcc
	v_mul_lo_u32 v7, v5, v3
	v_add_u32_e32 v5, v7, v5
	v_cmp_ne_u32_e32 vcc, v6, v5
	s_and_saveexec_b64 s[8:9], vcc
	s_xor_b64 s[8:9], exec, s[8:9]
	s_cbranch_execz .LBB0_482
	v_readlane_b32 s10, v253, 61
	v_readlane_b32 s11, v253, 62
	s_waitcnt lgkmcnt(0)
	s_nop 3
	global_load_dword v2, v4, s[10:11] sc1
	s_waitcnt vmcnt(0)
	v_cmp_eq_u32_e32 vcc, v2, v3
	s_and_saveexec_b64 s[10:11], vcc
	s_cbranch_execz .LBB0_481
	s_mov_b32 s40, 1
	s_mov_b64 s[12:13], 0
	s_branch .LBB0_472

.LBB0_474:
	v_readlane_b32 s16, v253, 61
	v_readlane_b32 s17, v253, 62
	s_add_i32 s40, s40, 1
	s_mov_b64 s[18:19], -1
	s_nop 2
	global_load_dword v2, v4, s[16:17] sc1
	s_waitcnt vmcnt(0)
	v_cmp_ne_u32_e32 vcc, v2, v3
	s_orn2_b64 s[16:17], vcc, exec
	s_branch .LBB0_471
